# attention main loop: static priority raise for waves 0-3 instead of 4-7
# speedup vs baseline: 1.0005x; 1.0005x over previous
; __global__ void __launch_bounds__(NWAVES * 64, 2) mega_fwd(Args args) {
;     ...
;                 if (F.tid == 0) QS[0] = (int)__hip_atomic_fetch_add(F.ctl + CW_Q + 64 * F.l + 4 * pa_, 1u, __ATOMIC_RELAXED, __HIP_MEMORY_SCOPE_AGENT);
;                 __syncthreads();
;                 const int idx = __builtin_amdgcn_readfirstlane(QS[0]);
;                 __syncthreads();
;                 if (idx >= ((QMODE >= 2) ? 512 : 512 + 2560)) break;
;                 if (idx < 512) { const attn_body::AttnUnit u{(idx & 3) * 4 + 3 - ((idx >> 2) & 3), 31 - (idx >> 4)};
;                     attn_body::attn_unit<8>(u.bh / 4, u.bh % 4, u.qb, AT.Q, AT.K, AT.V, AT.O, AT.F2, AT.gain, 2.0f * sqrtf(__uint_as_float(AT.qkn[2 * u.bh]) * __uint_as_float(AT.qkn[2 * u.bh + 1])), (char*)lds); }
.LBB0_2757:
	s_or_b64 exec, exec, s[0:1]
	v_mov_b32_e32 v0, s17
	s_waitcnt vmcnt(0) lgkmcnt(0)
	s_barrier
	ds_read_b32 v0, v0
	s_mov_b64 s[0:1], -1
	s_waitcnt lgkmcnt(0)
	s_barrier
	v_readfirstlane_b32 s4, v0
	s_cmpk_gt_i32 s4, 0x1ff
	s_cbranch_scc1 .LBB0_2752
	v_readfirstlane_b32 s62, v228
	s_cmp_gt_u32 s62, 255
	s_cbranch_scc1 .Lmy_att_noprio
	s_setprio 1
